# row max as 4 independent v_max3 chains instead of one 64-deep chain (on top of last-iteration K-prefetch skip)
# baseline (speedup 1.0000x reference)
.LBB1_14:
	s_and_b32 s24, s12, 24
	s_or_b32 s56, s24, s27
	s_and_b32 s24, s57, 1
	s_or_b32 s55, s24, s28
	s_add_i32 s24, s55, s29
	s_lshl_b32 s24, s24, 12
	s_lshl_b32 s58, s56, 18
	ds_read_b128 v[64:67], v243
	ds_read_b128 v[68:71], v243 offset:16
	s_waitcnt lgkmcnt(1)
	v_pk_mul_f32 v[76:77], v[64:65], s[22:23] op_sel_hi:[1,0]
	s_waitcnt lgkmcnt(0)
	v_pk_mul_f32 v[64:65], v[68:69], s[22:23] op_sel_hi:[1,0]
	v_pk_mul_f32 v[78:79], v[66:67], s[22:23] op_sel_hi:[1,0]
	v_pk_mul_f32 v[74:75], v[70:71], s[22:23] op_sel_hi:[1,0]
	v_cvt_pk_f16_f32 v204, v64, v65
	ds_read_b128 v[64:67], v243 offset:64
	ds_read_b128 v[68:71], v243 offset:80
	v_cvt_pk_f16_f32 v202, v76, v77
	v_cvt_pk_f16_f32 v205, v74, v75
	v_cvt_pk_f16_f32 v203, v78, v79
	s_waitcnt lgkmcnt(1)
	v_pk_mul_f32 v[76:77], v[64:65], s[22:23] op_sel_hi:[1,0]
	s_waitcnt lgkmcnt(0)
	v_pk_mul_f32 v[64:65], v[68:69], s[22:23] op_sel_hi:[1,0]
	v_pk_mul_f32 v[78:79], v[66:67], s[22:23] op_sel_hi:[1,0]
	v_pk_mul_f32 v[74:75], v[70:71], s[22:23] op_sel_hi:[1,0]
	v_cvt_pk_f16_f32 v208, v64, v65
	ds_read_b128 v[64:67], v243 offset:128
	ds_read_b128 v[68:71], v243 offset:144
	v_cvt_pk_f16_f32 v206, v76, v77
	v_cvt_pk_f16_f32 v209, v74, v75
	v_cvt_pk_f16_f32 v207, v78, v79
	s_waitcnt lgkmcnt(1)
	v_pk_mul_f32 v[76:77], v[64:65], s[22:23] op_sel_hi:[1,0]
	s_waitcnt lgkmcnt(0)
	v_pk_mul_f32 v[64:65], v[68:69], s[22:23] op_sel_hi:[1,0]
	v_pk_mul_f32 v[78:79], v[66:67], s[22:23] op_sel_hi:[1,0]
	v_pk_mul_f32 v[74:75], v[70:71], s[22:23] op_sel_hi:[1,0]
	v_cvt_pk_f16_f32 v212, v64, v65
	ds_read_b128 v[64:67], v243 offset:192
	ds_read_b128 v[68:71], v243 offset:208
	v_cvt_pk_f16_f32 v211, v78, v79
	v_cvt_pk_f16_f32 v210, v76, v77
	v_cvt_pk_f16_f32 v213, v74, v75
	s_waitcnt lgkmcnt(1)
	v_pk_mul_f32 v[78:79], v[66:67], s[22:23] op_sel_hi:[1,0]
	s_waitcnt lgkmcnt(0)
	v_pk_mul_f32 v[66:67], v[70:71], s[22:23] op_sel_hi:[1,0]
	v_pk_mul_f32 v[64:65], v[64:65], s[22:23] op_sel_hi:[1,0]
	v_pk_mul_f32 v[68:69], v[68:69], s[22:23] op_sel_hi:[1,0]
	v_cvt_pk_f16_f32 v214, v64, v65
	v_cvt_pk_f16_f32 v216, v68, v69
	v_cvt_pk_f16_f32 v217, v66, v67
	v_cvt_pk_f16_f32 v215, v78, v79
	s_waitcnt vmcnt(57)
	v_mfma_f32_32x32x16_f16 v[112:127], v[48:51], v[202:205], 0
	v_mfma_f32_32x32x16_f16 v[112:127], v[52:55], v[206:209], v[112:127]
	v_mfma_f32_32x32x16_f16 v[112:127], v[56:59], v[210:213], v[112:127]
	v_mfma_f32_32x32x16_f16 v[112:127], v[60:63], v[214:217], v[112:127]
	s_waitcnt vmcnt(50)
	v_mfma_f32_32x32x16_f16 v[48:63], v[32:35], v[202:205], 0
	s_waitcnt vmcnt(49)
	v_mfma_f32_32x32x16_f16 v[48:63], v[36:39], v[206:209], v[48:63]
	v_mfma_f32_32x32x16_f16 v[48:63], v[40:43], v[210:213], v[48:63]
	v_mfma_f32_32x32x16_f16 v[48:63], v[44:47], v[214:217], v[48:63]
	s_waitcnt vmcnt(48)
	v_mfma_f32_32x32x16_f16 v[32:47], v[16:19], v[202:205], 0
	s_waitcnt vmcnt(47)
	v_mfma_f32_32x32x16_f16 v[32:47], v[20:23], v[206:209], v[32:47]
	s_waitcnt vmcnt(46)
	v_mfma_f32_32x32x16_f16 v[32:47], v[24:27], v[210:213], v[32:47]
	s_waitcnt vmcnt(45)
	v_mfma_f32_32x32x16_f16 v[32:47], v[28:31], v[214:217], v[32:47]
	s_waitcnt vmcnt(44)
	v_mfma_f32_32x32x16_f16 v[16:31], v[4:7], v[202:205], 0
	s_waitcnt vmcnt(43)
	v_mfma_f32_32x32x16_f16 v[16:31], v[8:11], v[206:209], v[16:31]
	s_waitcnt vmcnt(42)
	v_mfma_f32_32x32x16_f16 v[16:31], v[12:15], v[210:213], v[16:31]
	v_mfma_f32_32x32x16_f16 v[16:31], v[148:151], v[214:217], v[16:31]
	v_mfma_f32_32x32x16_f16 v[0:15], v[132:135], v[202:205], 0
	v_mfma_f32_32x32x16_f16 v[0:15], v[136:139], v[206:209], v[0:15]
	v_mfma_f32_32x32x16_f16 v[0:15], v[140:143], v[210:213], v[0:15]
	v_mfma_f32_32x32x16_f16 v[0:15], v[144:147], v[214:217], v[0:15]
	s_waitcnt vmcnt(25)
	v_mfma_f32_32x32x16_f16 v[64:79], v[80:83], v[202:205], 0
	s_waitcnt vmcnt(24)
	v_mfma_f32_32x32x16_f16 v[64:79], v[84:87], v[206:209], v[64:79]
	s_waitcnt vmcnt(23)
	v_mfma_f32_32x32x16_f16 v[64:79], v[88:91], v[210:213], v[64:79]
	s_waitcnt vmcnt(22)
	v_mfma_f32_32x32x16_f16 v[64:79], v[92:95], v[214:217], v[64:79]
	s_waitcnt vmcnt(21)
	v_mfma_f32_32x32x16_f16 v[80:95], v[96:99], v[202:205], 0
	s_waitcnt vmcnt(20)
	v_mfma_f32_32x32x16_f16 v[80:95], v[100:103], v[206:209], v[80:95]
	s_waitcnt vmcnt(19)
	v_mfma_f32_32x32x16_f16 v[80:95], v[108:111], v[210:213], v[80:95]
	s_waitcnt vmcnt(18)
	v_mfma_f32_32x32x16_f16 v[80:95], v[192:195], v[214:217], v[80:95]
	v_mfma_f32_32x32x16_f16 v[96:111], v[152:155], v[202:205], 0
	v_mfma_f32_32x32x16_f16 v[96:111], v[156:159], v[206:209], v[96:111]
	s_waitcnt vmcnt(17)
	v_mfma_f32_32x32x16_f16 v[96:111], v[174:177], v[210:213], v[96:111]
	s_waitcnt vmcnt(16)
	v_mfma_f32_32x32x16_f16 v[96:111], v[178:181], v[214:217], v[96:111]
	s_and_b32 s25, s24, 0x3f000
	s_addk_i32 s24, 0x1000
	s_or_b32 s25, s58, s25
	s_and_b32 s24, s24, 0x3f000
	v_or_b32_e32 v132, s25, v231
	s_or_b32 s24, s58, s24
	global_load_dwordx4 v[156:159], v132, s[16:17]
	global_load_dwordx4 v[160:163], v132, s[16:17] offset:1024
	global_load_dwordx4 v[152:155], v132, s[16:17] offset:2048
	global_load_dwordx4 v[148:151], v132, s[16:17] offset:3072
	v_or_b32_e32 v132, s24, v231
	global_load_dwordx4 v[144:147], v132, s[16:17]
	global_load_dwordx4 v[140:143], v132, s[16:17] offset:1024
	global_load_dwordx4 v[136:139], v132, s[16:17] offset:2048
	s_nop 0
	global_load_dwordx4 v[132:135], v132, s[16:17] offset:3072
	v_max_f32_e32 v166, v113, v113
	v_max_f32_e32 v167, v112, v112
	v_max_f32_e32 v166, v167, v166
	v_max3_f32 v166, v166, v114, v115
	v_max_f32_e32 v167, v116, v117
	v_max_f32_e32 v202, v118, v119
	v_max_f32_e32 v203, v120, v121
	v_max3_f32 v166, v166, v122, v123
	v_max3_f32 v167, v167, v124, v125
	v_max3_f32 v202, v202, v126, v127
	v_max3_f32 v203, v203, v96, v97
	v_max3_f32 v166, v166, v98, v99
	v_max3_f32 v167, v167, v100, v101
	v_max3_f32 v202, v202, v102, v103
	v_max3_f32 v203, v203, v104, v105
	v_max3_f32 v166, v166, v106, v107
	v_max3_f32 v167, v167, v108, v109
	v_max3_f32 v202, v202, v110, v111
	v_max3_f32 v203, v203, v80, v81
	v_max3_f32 v166, v166, v82, v83
	v_max3_f32 v167, v167, v84, v85
	v_max3_f32 v202, v202, v86, v87
	v_max3_f32 v203, v203, v88, v89
	v_max3_f32 v166, v166, v90, v91
	v_max3_f32 v167, v167, v92, v93
	v_max3_f32 v202, v202, v94, v95
	v_max3_f32 v203, v203, v64, v65
	v_max3_f32 v166, v166, v66, v67
	v_max3_f32 v167, v167, v68, v69
	v_max3_f32 v202, v202, v70, v71
	v_max3_f32 v203, v203, v72, v73
	v_max3_f32 v166, v166, v74, v75
	v_max3_f32 v167, v167, v76, v77
	v_max3_f32 v202, v202, v78, v79
	v_max3_f32 v203, v203, v48, v49
	v_max3_f32 v166, v166, v50, v51
	v_max3_f32 v167, v167, v52, v53
	v_max3_f32 v202, v202, v54, v55
	v_max3_f32 v203, v203, v56, v57
	v_max3_f32 v166, v166, v58, v59
	v_max3_f32 v167, v167, v60, v61
	v_max3_f32 v202, v202, v62, v63
	v_max3_f32 v203, v203, v32, v33
	v_max3_f32 v166, v166, v34, v35
	v_max3_f32 v167, v167, v36, v37
	v_max3_f32 v202, v202, v38, v39
	v_max3_f32 v203, v203, v40, v41
	v_max3_f32 v166, v166, v42, v43
	v_max3_f32 v167, v167, v44, v45
	v_max3_f32 v202, v202, v46, v47
	v_max3_f32 v203, v203, v16, v17
	v_max3_f32 v166, v166, v18, v19
	v_max3_f32 v167, v167, v20, v21
	v_max3_f32 v202, v202, v22, v23
	v_max3_f32 v203, v203, v24, v25
	v_max3_f32 v166, v166, v26, v27
	v_max3_f32 v167, v167, v28, v29
	v_max3_f32 v202, v202, v30, v31
	v_max3_f32 v203, v203, v0, v1
	v_max3_f32 v166, v166, v2, v3
	v_max3_f32 v167, v167, v4, v5
	v_max3_f32 v202, v202, v6, v7
	v_max3_f32 v203, v203, v8, v9
	v_max3_f32 v166, v166, v10, v11
	v_max3_f32 v167, v167, v12, v13
	v_max3_f32 v202, v202, v14, v15
	v_max3_f32 v166, v166, v167, v202
	v_max_f32_e32 v166, v166, v203
	ds_bpermute_b32 v167, v234, v166
	s_waitcnt lgkmcnt(0)
	v_max_f32_e32 v167, v167, v167
	v_max_f32_e32 v247, v166, v167
	s_and_saveexec_b64 s[24:25], s[0:1]
	v_add_u32_e32 v166, s31, v235
	ds_write_b32 v166, v247
	s_or_b64 exec, exec, s[24:25]
	v_sub_f32_e32 v112, v112, v247
	v_exp_f32_e32 v208, v112
	v_sub_f32_e32 v112, v113, v247
	v_exp_f32_e32 v209, v112
	v_sub_f32_e32 v112, v114, v247
	v_exp_f32_e32 v204, v112
	v_sub_f32_e32 v112, v115, v247
	v_exp_f32_e32 v205, v112
	v_sub_f32_e32 v113, v116, v247
	v_add_f32_e32 v112, 0, v208
	v_exp_f32_e32 v182, v113
	v_sub_f32_e32 v113, v117, v247
	v_add_f32_e32 v112, v112, v209
	v_exp_f32_e32 v183, v113
	v_sub_f32_e32 v113, v118, v247
	v_add_f32_e32 v112, v112, v204
	v_exp_f32_e32 v178, v113
	v_sub_f32_e32 v113, v119, v247
	v_add_f32_e32 v112, v112, v205
	v_exp_f32_e32 v179, v113
	v_sub_f32_e32 v113, v120, v247
	v_add_f32_e32 v112, v112, v182
	v_exp_f32_e32 v166, v113
	v_sub_f32_e32 v113, v121, v247
	v_add_f32_e32 v112, v112, v183
	v_exp_f32_e32 v167, v113
	v_sub_f32_e32 v113, v122, v247
	v_add_f32_e32 v112, v112, v178
	v_exp_f32_e32 v118, v113
	v_sub_f32_e32 v113, v123, v247
	v_add_f32_e32 v112, v112, v179
	v_exp_f32_e32 v119, v113
	v_sub_f32_e32 v113, v124, v247
	v_add_f32_e32 v112, v112, v166
	v_exp_f32_e32 v116, v113
	v_sub_f32_e32 v113, v125, v247
	v_add_f32_e32 v112, v112, v167
	v_exp_f32_e32 v117, v113
	v_sub_f32_e32 v113, v126, v247
	v_add_f32_e32 v112, v112, v118
	v_exp_f32_e32 v114, v113
	v_sub_f32_e32 v113, v127, v247
	v_add_f32_e32 v112, v112, v119
	v_exp_f32_e32 v115, v113
	v_add_f32_e32 v112, v112, v116
	v_add_f32_e32 v112, v112, v117
	v_add_f32_e32 v112, v112, v114
	v_sub_f32_e32 v96, v96, v247
	v_add_f32_e32 v120, v112, v115
	v_exp_f32_e32 v112, v96
	v_sub_f32_e32 v96, v97, v247
	v_exp_f32_e32 v113, v96
	v_sub_f32_e32 v96, v98, v247
	v_exp_f32_e32 v98, v96
	v_sub_f32_e32 v96, v99, v247
	v_exp_f32_e32 v99, v96
	v_sub_f32_e32 v97, v100, v247
	v_add_f32_e32 v96, v120, v112
	v_exp_f32_e32 v100, v97
	v_sub_f32_e32 v97, v101, v247
	v_add_f32_e32 v96, v96, v113
	v_exp_f32_e32 v101, v97
	v_sub_f32_e32 v97, v102, v247
	v_add_f32_e32 v96, v96, v98
	v_exp_f32_e32 v120, v97
	v_sub_f32_e32 v97, v103, v247
	v_add_f32_e32 v96, v96, v99
	v_exp_f32_e32 v121, v97
	v_sub_f32_e32 v97, v104, v247
	v_add_f32_e32 v96, v96, v100
	v_exp_f32_e32 v102, v97
	v_sub_f32_e32 v97, v105, v247
	v_add_f32_e32 v96, v96, v101
	v_exp_f32_e32 v103, v97
	v_sub_f32_e32 v97, v106, v247
	v_add_f32_e32 v96, v96, v120
	v_exp_f32_e32 v122, v97
	v_sub_f32_e32 v97, v107, v247
	v_add_f32_e32 v96, v96, v121
	v_exp_f32_e32 v123, v97
	v_sub_f32_e32 v97, v108, v247
	v_add_f32_e32 v96, v96, v102
	v_exp_f32_e32 v124, v97
	v_sub_f32_e32 v97, v109, v247
	v_add_f32_e32 v96, v96, v103
	v_exp_f32_e32 v125, v97
	v_sub_f32_e32 v97, v110, v247
	v_add_f32_e32 v96, v96, v122
	v_exp_f32_e32 v180, v97
	v_sub_f32_e32 v97, v111, v247
	v_add_f32_e32 v96, v96, v123
	v_exp_f32_e32 v181, v97
	v_sub_f32_e32 v80, v80, v247
	v_add_f32_e32 v96, v96, v124
	v_exp_f32_e32 v80, v80
	v_sub_f32_e32 v81, v81, v247
	v_add_f32_e32 v96, v96, v125
	v_exp_f32_e32 v81, v81
	v_sub_f32_e32 v82, v82, v247
	v_add_f32_e32 v96, v96, v180
	v_exp_f32_e32 v82, v82
	v_sub_f32_e32 v83, v83, v247
	v_add_f32_e32 v96, v96, v181
	v_exp_f32_e32 v83, v83
	v_add_f32_e32 v96, v96, v80
	v_sub_f32_e32 v84, v84, v247
	v_add_f32_e32 v96, v96, v81
	v_exp_f32_e32 v84, v84
	v_sub_f32_e32 v85, v85, v247
	v_add_f32_e32 v96, v96, v82
	v_exp_f32_e32 v85, v85
	v_sub_f32_e32 v86, v86, v247
	v_add_f32_e32 v104, v96, v83
	v_exp_f32_e32 v96, v86
	v_sub_f32_e32 v86, v87, v247
	v_exp_f32_e32 v97, v86
	v_add_f32_e32 v86, v104, v84
	v_add_f32_e32 v86, v86, v85
	v_add_f32_e32 v86, v86, v96
	v_add_f32_e32 v104, v86, v97
	v_sub_f32_e32 v86, v88, v247
	v_exp_f32_e32 v86, v86
	v_sub_f32_e32 v87, v89, v247
	v_exp_f32_e32 v87, v87
	v_sub_f32_e32 v88, v90, v247
	v_exp_f32_e32 v88, v88
	v_sub_f32_e32 v89, v91, v247
	v_exp_f32_e32 v89, v89
	v_add_f32_e32 v90, v104, v86
	v_add_f32_e32 v90, v90, v87
	v_add_f32_e32 v90, v90, v88
	v_add_f32_e32 v104, v90, v89
	v_sub_f32_e32 v90, v92, v247
	v_exp_f32_e32 v90, v90
	v_sub_f32_e32 v91, v93, v247
	v_exp_f32_e32 v91, v91
	v_sub_f32_e32 v92, v94, v247
	v_exp_f32_e32 v94, v92
	v_sub_f32_e32 v92, v95, v247
	v_exp_f32_e32 v95, v92
	v_add_f32_e32 v92, v104, v90
	v_add_f32_e32 v92, v92, v91
	v_add_f32_e32 v92, v92, v94
	v_sub_f32_e32 v64, v64, v247
	v_add_f32_e32 v104, v92, v95
	v_exp_f32_e32 v92, v64
	v_sub_f32_e32 v64, v65, v247
	v_exp_f32_e32 v93, v64
	v_sub_f32_e32 v64, v66, v247
	v_exp_f32_e32 v108, v64
	v_sub_f32_e32 v64, v67, v247
	v_exp_f32_e32 v109, v64
	v_sub_f32_e32 v65, v68, v247
	v_add_f32_e32 v64, v104, v92
	v_exp_f32_e32 v110, v65
	v_sub_f32_e32 v65, v69, v247
	v_add_f32_e32 v64, v64, v93
	v_exp_f32_e32 v111, v65
	v_sub_f32_e32 v65, v70, v247
	v_add_f32_e32 v64, v64, v108
	v_exp_f32_e32 v176, v65
	v_sub_f32_e32 v65, v71, v247
	v_add_f32_e32 v64, v64, v109
	v_exp_f32_e32 v177, v65
	v_sub_f32_e32 v65, v72, v247
	v_add_f32_e32 v64, v64, v110
	v_exp_f32_e32 v174, v65
	v_sub_f32_e32 v65, v73, v247
	v_add_f32_e32 v64, v64, v111
	v_exp_f32_e32 v175, v65
	v_sub_f32_e32 v65, v74, v247
	v_add_f32_e32 v64, v64, v176
	v_exp_f32_e32 v192, v65
	v_sub_f32_e32 v65, v75, v247
	v_add_f32_e32 v64, v64, v177
	v_exp_f32_e32 v193, v65
	v_sub_f32_e32 v65, v76, v247
	v_add_f32_e32 v64, v64, v174
	v_exp_f32_e32 v194, v65
	v_sub_f32_e32 v65, v77, v247
	v_add_f32_e32 v64, v64, v175
	v_exp_f32_e32 v195, v65
	v_sub_f32_e32 v65, v78, v247
	v_add_f32_e32 v64, v64, v192
	v_exp_f32_e32 v206, v65
	v_sub_f32_e32 v65, v79, v247
	v_add_f32_e32 v64, v64, v193
	v_exp_f32_e32 v207, v65
	v_add_f32_e32 v64, v64, v194
	v_add_f32_e32 v64, v64, v195
	v_add_f32_e32 v64, v64, v206
	v_sub_f32_e32 v48, v48, v247
	v_add_f32_e32 v68, v64, v207
	v_exp_f32_e32 v64, v48
	v_sub_f32_e32 v48, v49, v247
	v_exp_f32_e32 v65, v48
	v_sub_f32_e32 v48, v50, v247
	v_exp_f32_e32 v66, v48
	v_sub_f32_e32 v48, v51, v247
	v_exp_f32_e32 v67, v48
	v_sub_f32_e32 v49, v52, v247
	v_add_f32_e32 v48, v68, v64
	v_exp_f32_e32 v68, v49
	v_sub_f32_e32 v49, v53, v247
	v_add_f32_e32 v48, v48, v65
	v_exp_f32_e32 v69, v49
	v_sub_f32_e32 v49, v54, v247
	v_add_f32_e32 v48, v48, v66
	v_exp_f32_e32 v74, v49
	v_sub_f32_e32 v49, v55, v247
	v_add_f32_e32 v48, v48, v67
	v_exp_f32_e32 v75, v49
	v_sub_f32_e32 v49, v56, v247
	v_add_f32_e32 v48, v48, v68
	v_exp_f32_e32 v72, v49
	v_sub_f32_e32 v49, v57, v247
	v_add_f32_e32 v48, v48, v69
	v_exp_f32_e32 v73, v49
	v_sub_f32_e32 v49, v58, v247
	v_add_f32_e32 v48, v48, v74
	v_exp_f32_e32 v104, v49
	v_sub_f32_e32 v49, v59, v247
	v_add_f32_e32 v48, v48, v75
	v_exp_f32_e32 v105, v49
	v_sub_f32_e32 v49, v60, v247
	v_add_f32_e32 v48, v48, v72
	v_exp_f32_e32 v106, v49
	v_sub_f32_e32 v49, v61, v247
	v_add_f32_e32 v48, v48, v73
	v_exp_f32_e32 v107, v49
	v_sub_f32_e32 v49, v62, v247
	v_add_f32_e32 v48, v48, v104
	v_exp_f32_e32 v172, v49
	v_sub_f32_e32 v49, v63, v247
	v_add_f32_e32 v48, v48, v105
	v_exp_f32_e32 v173, v49
	v_sub_f32_e32 v32, v32, v247
	v_add_f32_e32 v48, v48, v106
	v_exp_f32_e32 v170, v32
	v_sub_f32_e32 v32, v33, v247
	v_add_f32_e32 v48, v48, v107
	v_exp_f32_e32 v171, v32
	v_sub_f32_e32 v32, v34, v247
	v_add_f32_e32 v48, v48, v172
	v_exp_f32_e32 v188, v32
	v_sub_f32_e32 v32, v35, v247
	v_add_f32_e32 v48, v48, v173
	v_exp_f32_e32 v189, v32
	v_sub_f32_e32 v33, v36, v247
	v_add_f32_e32 v32, v48, v170
	v_exp_f32_e32 v190, v33
	v_sub_f32_e32 v33, v37, v247
	v_add_f32_e32 v32, v32, v171
	v_exp_f32_e32 v191, v33
	v_sub_f32_e32 v33, v38, v247
	v_add_f32_e32 v32, v32, v188
	v_exp_f32_e32 v202, v33
	v_sub_f32_e32 v33, v39, v247
	v_add_f32_e32 v32, v32, v189
	v_exp_f32_e32 v203, v33
	v_sub_f32_e32 v33, v40, v247
	v_add_f32_e32 v32, v32, v190
	v_exp_f32_e32 v200, v33
	v_sub_f32_e32 v33, v41, v247
	v_add_f32_e32 v32, v32, v191
	v_exp_f32_e32 v201, v33
	v_sub_f32_e32 v33, v42, v247
	v_add_f32_e32 v32, v32, v202
	v_exp_f32_e32 v214, v33
	v_sub_f32_e32 v33, v43, v247
	v_add_f32_e32 v32, v32, v203
	v_exp_f32_e32 v215, v33
	v_sub_f32_e32 v33, v44, v247
	v_add_f32_e32 v32, v32, v200
	v_exp_f32_e32 v216, v33
	v_sub_f32_e32 v33, v45, v247
	v_add_f32_e32 v32, v32, v201
	v_exp_f32_e32 v217, v33
	v_sub_f32_e32 v33, v46, v247
	v_add_f32_e32 v32, v32, v214
	v_exp_f32_e32 v222, v33
	v_sub_f32_e32 v33, v47, v247
	v_add_f32_e32 v32, v32, v215
	v_exp_f32_e32 v223, v33
	v_sub_f32_e32 v16, v16, v247
	v_add_f32_e32 v32, v32, v216
	v_exp_f32_e32 v70, v16
	v_sub_f32_e32 v16, v17, v247
	v_add_f32_e32 v32, v32, v217
	v_exp_f32_e32 v71, v16
	v_sub_f32_e32 v16, v18, v247
	v_add_f32_e32 v32, v32, v222
	v_exp_f32_e32 v76, v16
	v_sub_f32_e32 v16, v19, v247
	v_add_f32_e32 v32, v32, v223
	v_exp_f32_e32 v77, v16
	v_sub_f32_e32 v17, v20, v247
	v_add_f32_e32 v16, v32, v70
	v_exp_f32_e32 v78, v17
	v_sub_f32_e32 v17, v21, v247
	v_add_f32_e32 v16, v16, v71
	v_exp_f32_e32 v79, v17
	v_sub_f32_e32 v17, v22, v247
	v_add_f32_e32 v16, v16, v76
	v_exp_f32_e32 v168, v17
	v_sub_f32_e32 v17, v23, v247
	v_add_f32_e32 v16, v16, v77
	v_exp_f32_e32 v169, v17
	v_sub_f32_e32 v17, v24, v247
	v_add_f32_e32 v16, v16, v78
	v_exp_f32_e32 v126, v17
	v_sub_f32_e32 v17, v25, v247
	v_add_f32_e32 v16, v16, v79
	v_exp_f32_e32 v127, v17
	v_sub_f32_e32 v17, v26, v247
	v_add_f32_e32 v16, v16, v168
	v_exp_f32_e32 v184, v17
	v_sub_f32_e32 v17, v27, v247
	v_add_f32_e32 v16, v16, v169
	v_exp_f32_e32 v185, v17
	v_sub_f32_e32 v17, v28, v247
	v_add_f32_e32 v16, v16, v126
	v_exp_f32_e32 v186, v17
	v_sub_f32_e32 v17, v29, v247
	v_add_f32_e32 v16, v16, v127
	v_exp_f32_e32 v187, v17
	v_sub_f32_e32 v17, v30, v247
	v_add_f32_e32 v16, v16, v184
	v_exp_f32_e32 v198, v17
	v_sub_f32_e32 v17, v31, v247
	v_add_f32_e32 v16, v16, v185
	v_exp_f32_e32 v199, v17
	v_sub_f32_e32 v0, v0, v247
	v_add_f32_e32 v16, v16, v186
	v_exp_f32_e32 v196, v0
	v_sub_f32_e32 v0, v1, v247
	v_add_f32_e32 v16, v16, v187
	v_exp_f32_e32 v197, v0
	v_sub_f32_e32 v0, v2, v247
	v_add_f32_e32 v16, v16, v198
	v_exp_f32_e32 v210, v0
	v_sub_f32_e32 v0, v3, v247
	v_add_f32_e32 v16, v16, v199
	v_exp_f32_e32 v211, v0
	v_sub_f32_e32 v1, v4, v247
	v_add_f32_e32 v0, v16, v196
	v_exp_f32_e32 v212, v1
	v_sub_f32_e32 v1, v5, v247
	v_add_f32_e32 v0, v0, v197
	v_exp_f32_e32 v213, v1
	v_sub_f32_e32 v1, v6, v247
	v_add_f32_e32 v0, v0, v210
	v_exp_f32_e32 v220, v1
	v_sub_f32_e32 v1, v7, v247
	v_add_f32_e32 v0, v0, v211
	v_exp_f32_e32 v221, v1
	v_sub_f32_e32 v1, v8, v247
	v_add_f32_e32 v0, v0, v212
	v_exp_f32_e32 v218, v1
	v_sub_f32_e32 v1, v9, v247
	v_add_f32_e32 v0, v0, v213
	v_exp_f32_e32 v219, v1
	v_sub_f32_e32 v1, v10, v247
	v_add_f32_e32 v0, v0, v220
	v_exp_f32_e32 v224, v1
	v_sub_f32_e32 v1, v11, v247
	v_add_f32_e32 v0, v0, v221
	v_exp_f32_e32 v225, v1
	v_sub_f32_e32 v1, v12, v247
	v_add_f32_e32 v0, v0, v218
	v_exp_f32_e32 v226, v1
	v_sub_f32_e32 v1, v13, v247
	v_add_f32_e32 v0, v0, v219
	v_exp_f32_e32 v227, v1
	v_sub_f32_e32 v1, v14, v247
	v_add_f32_e32 v0, v0, v224
	v_exp_f32_e32 v228, v1
	v_sub_f32_e32 v1, v15, v247
	v_add_f32_e32 v0, v0, v225
	v_exp_f32_e32 v229, v1
	v_add_f32_e32 v0, v0, v226
	v_add_f32_e32 v0, v0, v227
	v_add_f32_e32 v0, v0, v228
	v_add_f32_e32 v0, v0, v229
	ds_bpermute_b32 v1, v234, v0
	s_and_saveexec_b64 s[24:25], s[0:1]
	s_cbranch_execz .LBB1_18
	s_waitcnt lgkmcnt(0)
	v_add_f32_e32 v0, v0, v1
	v_add_u32_e32 v1, s31, v236
	ds_write_b32 v1, v0
